# v59 + down-projection GEMM: padding rows of a unit's A operand (never-read outputs) fetched from the unit's first row instead of their own
# speedup vs baseline: 1.0060x; 1.0015x over previous
.LBB0_1040:
	s_lshl_b32 s0, s24, 2
	s_add_i32 s0, s0, 0
	s_add_i32 s0, s0, 0x20400
	v_mov_b32_e32 v1, s0
	ds_read2_b32 v[68:69], v1 offset0:32 offset1:64
	ds_read_b32 v70, v1
	ds_read_b32 v1, v1 offset:384
	s_mov_b64 s[36:37], -1
	s_waitcnt lgkmcnt(0)
	v_readfirstlane_b32 s0, v68
	v_readfirstlane_b32 s98, v70
	s_abs_i32 s25, s0
	v_cvt_f32_u32_e32 v68, s25
	v_readfirstlane_b32 s26, v1
	s_lshl_b32 s26, s26, 3
	s_sub_i32 s23, s23, s26
	v_rcp_iflag_f32_e32 v1, v68
	s_sub_i32 s26, 0, s25
	s_ashr_i32 s28, s23, 31
	s_abs_i32 s23, s23
	v_mul_f32_e32 v1, 0x4f7ffffe, v1
	v_cvt_u32_f32_e32 v1, v1
	s_ashr_i32 s0, s0, 31
	s_xor_b32 s0, s28, s0
	v_readfirstlane_b32 s27, v69
	v_readfirstlane_b32 s29, v1
	s_mul_i32 s26, s26, s29
	s_mul_hi_u32 s26, s29, s26
	s_add_i32 s29, s29, s26
	s_mul_hi_u32 s26, s23, s29
	s_mul_i32 s29, s26, s25
	s_sub_i32 s23, s23, s29
	s_add_i32 s30, s26, 1
	s_sub_i32 s29, s23, s25
	s_cmp_ge_u32 s23, s25
	s_cselect_b32 s26, s30, s26
	s_cselect_b32 s23, s29, s23
	s_add_i32 s29, s26, 1
	s_sub_i32 s30, s23, s25
	s_cmp_ge_u32 s23, s25
	s_cselect_b32 s25, s29, s26
	s_cselect_b32 s23, s30, s23
	s_xor_b32 s25, s25, s0
	s_sub_i32 s26, s25, s0
	s_xor_b32 s0, s23, s28
	s_sub_i32 s0, s0, s28
	s_lshl_b32 s0, s0, 8
	s_ashr_i32 s25, s24, 31
	s_add_i32 s62, s0, s27
	s_sub_i32 s98, s98, s0
	s_lshl_b64 s[28:29], s[24:25], 22
	s_add_u32 s0, s21, s28
	s_addc_u32 s23, s33, s29
	s_ashr_i32 s27, s26, 31
	s_lshl_b64 s[28:29], s[26:27], 19
	s_add_u32 s28, s0, s28
	s_addc_u32 s29, s23, s29
	s_mov_b32 s0, s24
	s_branch .LBB0_1042

.LBB0_1042:
	s_xor_b64 s[30:31], s[36:37], -1
	s_mov_b64 s[38:39], 0x700
	s_and_b64 vcc, exec, s[30:31]
	v_mov_b32_e32 v135, v3
	v_mov_b32_e32 v134, v2
	v_mov_b32_e32 v133, v152
	v_mov_b32_e32 v132, v0
	s_cbranch_vccnz .LBB0_1044
	v_mbcnt_lo_u32_b32 v1, -1, 0
	v_mbcnt_hi_u32_b32 v1, -1, v1
	v_readlane_b32 s23, v255, 4
	s_mov_b64 s[38:39], 0
	s_nop 0
	v_add_u32_e32 v1, s23, v1
	s_add_i32 s23, s62, 0x80
	v_ashrrev_i32_e32 v69, 31, v1
	v_lshrrev_b32_e32 v69, 26, v69
	v_lshlrev_b32_e32 v68, 4, v1
	v_add_u32_e32 v69, v1, v69
	v_bfe_i32 v1, v1, 27, 1
	v_lshrrev_b32_e32 v1, 22, v1
	v_add_u32_e32 v1, v68, v1
	v_and_b32_e32 v1, 0xfffffc00, v1
	v_sub_u32_e32 v1, v68, v1
	v_lshrrev_b32_e32 v70, 4, v1
	v_bitop3_b32 v70, v70, v1, 32 bitop3:0x6c
	v_ashrrev_i32_e32 v1, 31, v1
	v_ashrrev_i32_e32 v69, 6, v69
	v_lshrrev_b32_e32 v1, 26, v1
	v_lshlrev_b32_e32 v71, 3, v69
	v_add_u32_e32 v1, v70, v1
	v_and_b32_e32 v71, -16, v71
	v_ashrrev_i32_e32 v1, 6, v1
	v_add_u32_e32 v71, v1, v71
	v_mul_i32_i24_e32 v1, 64, v1
	v_sub_u32_e32 v1, v70, v1
	v_lshlrev_b32_e32 v69, 5, v69
	v_ashrrev_i16_sdwa v1, v159, sext(v1) dst_sel:DWORD dst_unused:UNUSED_PAD src0_sel:DWORD src1_sel:BYTE_0
	v_and_b32_e32 v69, 32, v69
	v_bfe_i32 v1, v1, 0, 16
	v_add_lshl_u32 v1, v69, v1, 1
	v_cmp_gt_u32_e32 vcc, s98, v71
	s_nop 1
	v_cndmask_b32_e32 v69, 0, v71, vcc
	v_add_u32_e32 v69, s62, v69
	v_lshl_add_u32 v132, v69, 11, v1
	v_add_u32_e32 v69, 0x80, v71
	v_cmp_gt_u32_e32 vcc, s98, v69
	s_nop 1
	v_cndmask_b32_e32 v69, 0, v69, vcc
	v_add_u32_e32 v69, s62, v69
	v_lshl_add_u32 v134, v69, 11, v1
	v_add_u32_e32 v1, 0x2000, v68
	v_ashrrev_i32_e32 v68, 31, v1
	v_lshrrev_b32_e32 v68, 22, v68
	v_add_u32_e32 v68, v1, v68
	v_ashrrev_i32_e32 v68, 10, v68
	v_mul_i32_i24_e32 v69, 0x400, v68
	v_sub_u32_e32 v1, v1, v69
	v_lshrrev_b32_e32 v69, 4, v1
	v_bitop3_b32 v1, v69, v1, 32 bitop3:0x6c
	v_ashrrev_i32_e32 v70, 31, v1
	v_lshrrev_b32_e32 v70, 26, v70
	v_add_u32_e32 v70, v1, v70
	v_ashrrev_i32_e32 v71, 6, v70
	v_and_b32_e32 v70, 0xc0, v70
	v_lshlrev_b32_e32 v69, 3, v68
	v_sub_u32_e32 v1, v1, v70
	v_and_b32_e32 v69, -16, v69
	v_lshlrev_b32_e32 v68, 5, v68
	v_ashrrev_i16_sdwa v1, v159, sext(v1) dst_sel:DWORD dst_unused:UNUSED_PAD src0_sel:DWORD src1_sel:BYTE_0
	v_add_u32_e32 v69, v71, v69
	v_and_b32_e32 v68, 32, v68
	v_bfe_i32 v1, v1, 0, 16
	v_add_lshl_u32 v1, v68, v1, 1
	v_cmp_gt_u32_e32 vcc, s98, v69
	s_nop 1
	v_cndmask_b32_e32 v68, 0, v69, vcc
	v_add_u32_e32 v68, s62, v68
	v_lshl_add_u32 v133, v68, 11, v1
	v_add_u32_e32 v68, 0x80, v69
	v_cmp_gt_u32_e32 vcc, s98, v68
	s_nop 1
	v_cndmask_b32_e32 v68, 0, v68, vcc
	v_add_u32_e32 v68, s62, v68
	v_lshl_add_u32 v135, v68, 11, v1
